# v59 + FFN-up epilogue stores non-temporal
# baseline (speedup 1.0000x reference)
.LBB0_2009:
	s_waitcnt vmcnt(0)
	v_ffbh_u32_e32 v161, v157
	v_min_u32_e32 v161, 32, v161
	v_lshlrev_b64 v[156:157], v161, v[156:157]
	v_min_u32_e32 v156, 1, v156
	v_or_b32_e32 v156, v157, v156
	v_cvt_f32_u32_e32 v156, v156
	v_sub_u32_e32 v157, 32, v161
	s_mov_b32 s36, 0x358637bd
	v_mov_b64_e32 v[166:167], s[36:37]
	v_ldexp_f32 v157, v156, v157
	v_ffbh_u32_e32 v156, v155
	v_min_u32_e32 v156, 32, v156
	v_lshlrev_b64 v[154:155], v156, v[154:155]
	v_min_u32_e32 v154, 1, v154
	v_or_b32_e32 v154, v155, v154
	v_cvt_f32_u32_e32 v154, v154
	v_sub_u32_e32 v155, 32, v156
	s_mov_b32 s40, 0x32800000
	s_mov_b32 s29, -1
	v_ldexp_f32 v156, v154, v155
	v_pk_fma_f32 v[154:155], v[156:157], s[40:41], v[166:167] op_sel_hi:[1,0,0]
	s_movk_i32 s95, 0x100
	v_mul_f32_e32 v156, 0x4b800000, v155
	v_cmp_gt_f32_e64 s[36:37], s96, v155
	v_cmp_gt_f32_e32 vcc, s96, v154
	v_mbcnt_lo_u32_b32 v0, s29, 0
	v_cndmask_b32_e64 v155, v155, v156, s[36:37]
	v_rsq_f32_e32 v155, v155
	v_mbcnt_hi_u32_b32 v159, s29, v0
	s_lshl_b32 s29, s58, 8
	v_lshrrev_b32_e32 v160, 1, v159
	v_mul_f32_e32 v156, 0x45800000, v155
	v_cndmask_b32_e64 v156, v155, v156, s[36:37]
	v_mul_f32_e32 v155, 0x4b800000, v154
	v_cndmask_b32_e32 v154, v154, v155, vcc
	v_rsq_f32_e32 v154, v154
	v_and_b32_e32 v0, 15, v159
	s_add_i32 s29, s29, s34
	v_and_b32_e32 v160, 56, v160
	v_mul_f32_e32 v155, 0x45800000, v154
	v_cndmask_b32_e32 v154, v154, v155, vcc
	v_ffbh_u32_e32 v155, v153
	v_min_u32_e32 v155, 32, v155
	v_lshlrev_b64 v[152:153], v155, v[152:153]
	v_min_u32_e32 v152, 1, v152
	v_or_b32_e32 v152, v153, v152
	v_cvt_f32_u32_e32 v152, v152
	v_sub_u32_e32 v153, 32, v155
	v_or_b32_e32 v158, s29, v0
	v_add_u32_e32 v160, s85, v160
	v_ldexp_f32 v153, v152, v153
	v_ffbh_u32_e32 v152, v151
	v_min_u32_e32 v152, 32, v152
	v_lshlrev_b64 v[150:151], v152, v[150:151]
	v_min_u32_e32 v150, 1, v150
	v_or_b32_e32 v150, v151, v150
	v_cvt_f32_u32_e32 v150, v150
	v_sub_u32_e32 v151, 32, v152
	s_cmp_gt_i32 s50, 15
	v_ldexp_f32 v152, v150, v151
	v_pk_fma_f32 v[150:151], v[152:153], s[40:41], v[166:167] op_sel_hi:[1,0,0]
	s_nop 0
	v_mul_f32_e32 v152, 0x4b800000, v151
	v_cmp_gt_f32_e64 s[36:37], s96, v151
	v_cmp_gt_f32_e32 vcc, s96, v150
	s_nop 0
	v_cndmask_b32_e64 v151, v151, v152, s[36:37]
	v_rsq_f32_e32 v151, v151
	s_nop 0
	v_mul_f32_e32 v152, 0x45800000, v151
	v_cndmask_b32_e64 v152, v151, v152, s[36:37]
	v_mul_f32_e32 v151, 0x4b800000, v150
	v_cndmask_b32_e32 v150, v150, v151, vcc
	v_rsq_f32_e32 v150, v150
	s_nop 0
	v_mul_f32_e32 v151, 0x45800000, v150
	v_cndmask_b32_e32 v150, v150, v151, vcc
	v_ffbh_u32_e32 v151, v149
	v_min_u32_e32 v151, 32, v151
	v_lshlrev_b64 v[148:149], v151, v[148:149]
	v_min_u32_e32 v148, 1, v148
	v_or_b32_e32 v148, v149, v148
	v_cvt_f32_u32_e32 v148, v148
	v_sub_u32_e32 v149, 32, v151
	v_ldexp_f32 v149, v148, v149
	v_ffbh_u32_e32 v148, v147
	v_min_u32_e32 v148, 32, v148
	v_lshlrev_b64 v[146:147], v148, v[146:147]
	v_min_u32_e32 v146, 1, v146
	v_or_b32_e32 v146, v147, v146
	v_cvt_f32_u32_e32 v146, v146
	v_sub_u32_e32 v147, 32, v148
	v_ldexp_f32 v148, v146, v147
	v_pk_fma_f32 v[146:147], v[148:149], s[40:41], v[166:167] op_sel_hi:[1,0,0]
	s_nop 0
	v_mul_f32_e32 v148, 0x4b800000, v147
	v_cmp_gt_f32_e64 s[36:37], s96, v147
	v_cmp_gt_f32_e32 vcc, s96, v146
	s_nop 0
	v_cndmask_b32_e64 v147, v147, v148, s[36:37]
	v_rsq_f32_e32 v147, v147
	s_nop 0
	v_mul_f32_e32 v148, 0x45800000, v147
	v_cndmask_b32_e64 v148, v147, v148, s[36:37]
	v_mul_f32_e32 v147, 0x4b800000, v146
	v_cndmask_b32_e32 v146, v146, v147, vcc
	v_rsq_f32_e32 v146, v146
	s_nop 0
	v_mul_f32_e32 v147, 0x45800000, v146
	v_cndmask_b32_e32 v146, v146, v147, vcc
	v_ffbh_u32_e32 v147, v145
	v_min_u32_e32 v147, 32, v147
	v_lshlrev_b64 v[144:145], v147, v[144:145]
	v_min_u32_e32 v144, 1, v144
	v_or_b32_e32 v144, v145, v144
	v_cvt_f32_u32_e32 v144, v144
	v_sub_u32_e32 v145, 32, v147
	v_ldexp_f32 v145, v144, v145
	v_ffbh_u32_e32 v144, v143
	v_min_u32_e32 v144, 32, v144
	v_lshlrev_b64 v[142:143], v144, v[142:143]
	v_min_u32_e32 v142, 1, v142
	v_or_b32_e32 v142, v143, v142
	v_cvt_f32_u32_e32 v142, v142
	v_sub_u32_e32 v143, 32, v144
	v_ldexp_f32 v144, v142, v143
	v_pk_fma_f32 v[142:143], v[144:145], s[40:41], v[166:167] op_sel_hi:[1,0,0]
	s_nop 0
	v_mul_f32_e32 v144, 0x4b800000, v143
	v_cmp_gt_f32_e64 s[36:37], s96, v143
	v_cmp_gt_f32_e32 vcc, s96, v142
	s_nop 0
	v_cndmask_b32_e64 v143, v143, v144, s[36:37]
	v_rsq_f32_e32 v143, v143
	s_nop 0
	v_mul_f32_e32 v144, 0x45800000, v143
	v_cndmask_b32_e64 v144, v143, v144, s[36:37]
	v_mul_f32_e32 v143, 0x4b800000, v142
	v_cndmask_b32_e32 v142, v142, v143, vcc
	v_rsq_f32_e32 v142, v142
	s_mov_b64 s[36:37], -1
	v_mul_f32_e32 v143, 0x45800000, v142
	v_cndmask_b32_e32 v142, v142, v143, vcc
	s_cbranch_scc0 .LBB0_2021
	s_cmp_gt_u32 s50, 19
	s_cbranch_scc0 .LBB0_2018
	s_and_b64 vcc, exec, s[38:39]
	s_cbranch_vccz .LBB0_2015
	v_readlane_b32 s36, v253, 45
	v_cmp_gt_u32_e32 vcc, 16, v159
	v_readlane_b32 s37, v253, 46
	s_and_b64 s[40:41], s[36:37], vcc
	s_and_saveexec_b64 s[36:37], s[40:41]
	s_cbranch_execz .LBB0_2014
	v_ashrrev_i32_e32 v159, 31, v158
	v_lshlrev_b64 v[166:167], 5, v[158:159]
	v_mul_f32_e32 v172, 0x3d3504f3, v156
	v_lshl_add_u64 v[170:171], s[42:43], 0, v[166:167]
	v_pk_mul_f32 v[168:169], v[172:173], v[128:129] op_sel_hi:[0,1]
	v_pk_mul_f32 v[166:167], v[172:173], v[126:127] op_sel_hi:[0,1]
	global_store_dwordx4 v[170:171], v[166:169], off sc1 nt
	v_mul_f32_e32 v174, 0x3d3504f3, v154
	s_mov_b64 s[40:41], 0x1000
	v_pk_mul_f32 v[168:169], v[172:173], v[124:125] op_sel_hi:[0,1]
	v_pk_mul_f32 v[166:167], v[172:173], v[122:123] op_sel_hi:[0,1]
	global_store_dwordx4 v[170:171], v[166:169], off offset:16 sc1 nt
	s_nop 1
	v_or_b32_e32 v166, 16, v158
	v_ashrrev_i32_e32 v167, 31, v166
	v_lshlrev_b64 v[166:167], 5, v[166:167]
	v_lshl_add_u64 v[172:173], s[42:43], 0, v[166:167]
	v_pk_mul_f32 v[168:169], v[174:175], v[116:117] op_sel_hi:[0,1]
	v_pk_mul_f32 v[166:167], v[174:175], v[114:115] op_sel_hi:[0,1]
	global_store_dwordx4 v[172:173], v[166:169], off sc1 nt
	s_nop 1
	v_pk_mul_f32 v[168:169], v[174:175], v[108:109] op_sel_hi:[0,1]
	v_pk_mul_f32 v[166:167], v[174:175], v[106:107] op_sel_hi:[0,1]
	global_store_dwordx4 v[172:173], v[166:169], off offset:16 sc1 nt
	v_mul_f32_e32 v174, 0x3d3504f3, v152
	s_nop 0
	v_or_b32_e32 v166, 32, v158
	v_ashrrev_i32_e32 v167, 31, v166
	v_lshlrev_b64 v[166:167], 5, v[166:167]
	v_lshl_add_u64 v[172:173], s[42:43], 0, v[166:167]
	v_pk_mul_f32 v[168:169], v[174:175], v[100:101] op_sel_hi:[0,1]
	v_pk_mul_f32 v[166:167], v[174:175], v[98:99] op_sel_hi:[0,1]
	global_store_dwordx4 v[172:173], v[166:169], off sc1 nt
	s_nop 1
	v_pk_mul_f32 v[168:169], v[174:175], v[92:93] op_sel_hi:[0,1]
	v_pk_mul_f32 v[166:167], v[174:175], v[90:91] op_sel_hi:[0,1]
	global_store_dwordx4 v[172:173], v[166:169], off offset:16 sc1 nt
	v_mul_f32_e32 v174, 0x3d3504f3, v150
	s_nop 0
	v_or_b32_e32 v166, 48, v158
	v_ashrrev_i32_e32 v167, 31, v166
	v_lshlrev_b64 v[166:167], 5, v[166:167]
	v_lshl_add_u64 v[172:173], s[42:43], 0, v[166:167]
	v_pk_mul_f32 v[168:169], v[174:175], v[84:85] op_sel_hi:[0,1]
	v_pk_mul_f32 v[166:167], v[174:175], v[82:83] op_sel_hi:[0,1]
	global_store_dwordx4 v[172:173], v[166:169], off sc1 nt
	s_nop 1
	v_pk_mul_f32 v[168:169], v[174:175], v[76:77] op_sel_hi:[0,1]
	v_pk_mul_f32 v[166:167], v[174:175], v[74:75] op_sel_hi:[0,1]
	global_store_dwordx4 v[172:173], v[166:169], off offset:16 sc1 nt
	v_lshl_add_u64 v[172:173], v[170:171], 0, s[40:41]
	s_movk_i32 s40, 0x1000
	v_mul_f32_e32 v174, 0x3d3504f3, v148
	v_add_co_u32_e32 v176, vcc, s40, v170
	v_pk_mul_f32 v[168:169], v[174:175], v[64:65] op_sel_hi:[0,1]
	v_pk_mul_f32 v[166:167], v[174:175], v[62:63] op_sel_hi:[0,1]
	v_addc_co_u32_e32 v177, vcc, 0, v171, vcc
	global_store_dwordx4 v[176:177], v[166:169], off sc1 nt
	s_mov_b64 s[40:41], 0x1200
	s_nop 0
	v_pk_mul_f32 v[168:169], v[174:175], v[60:61] op_sel_hi:[0,1]
	v_pk_mul_f32 v[166:167], v[174:175], v[58:59] op_sel_hi:[0,1]
	v_mul_f32_e32 v174, 0x3d3504f3, v146
	global_store_dwordx4 v[172:173], v[166:169], off offset:16 sc1 nt
	v_lshl_add_u64 v[172:173], v[170:171], 0, s[40:41]
	s_mov_b64 s[40:41], 0x1400
	v_pk_mul_f32 v[168:169], v[174:175], v[56:57] op_sel_hi:[0,1]
	v_pk_mul_f32 v[166:167], v[174:175], v[54:55] op_sel_hi:[0,1]
	global_store_dwordx4 v[176:177], v[166:169], off offset:512 sc1 nt
	s_nop 1
	v_pk_mul_f32 v[168:169], v[174:175], v[48:49] op_sel_hi:[0,1]
	v_pk_mul_f32 v[166:167], v[174:175], v[46:47] op_sel_hi:[0,1]
	v_mul_f32_e32 v174, 0x3d3504f3, v144
	global_store_dwordx4 v[172:173], v[166:169], off offset:16 sc1 nt
	v_lshl_add_u64 v[172:173], v[170:171], 0, s[40:41]
	s_mov_b64 s[40:41], 0x1600
	v_pk_mul_f32 v[168:169], v[174:175], v[40:41] op_sel_hi:[0,1]
	v_pk_mul_f32 v[166:167], v[174:175], v[38:39] op_sel_hi:[0,1]
	global_store_dwordx4 v[176:177], v[166:169], off offset:1024 sc1 nt
	v_lshl_add_u64 v[170:171], v[170:171], 0, s[40:41]
	s_nop 0
	v_pk_mul_f32 v[168:169], v[174:175], v[32:33] op_sel_hi:[0,1]
	v_pk_mul_f32 v[166:167], v[174:175], v[30:31] op_sel_hi:[0,1]
	global_store_dwordx4 v[172:173], v[166:169], off offset:16 sc1 nt
	v_mul_f32_e32 v172, 0x3d3504f3, v142
	s_nop 0
	v_pk_mul_f32 v[168:169], v[172:173], v[24:25] op_sel_hi:[0,1]
	v_pk_mul_f32 v[166:167], v[172:173], v[22:23] op_sel_hi:[0,1]
	global_store_dwordx4 v[176:177], v[166:169], off offset:1536 sc1 nt
	s_nop 1
	v_pk_mul_f32 v[168:169], v[172:173], v[16:17] op_sel_hi:[0,1]
	v_pk_mul_f32 v[166:167], v[172:173], v[14:15] op_sel_hi:[0,1]
	global_store_dwordx4 v[170:171], v[166:169], off offset:16 sc1 nt

.LBB0_2015:
	s_andn2_b64 vcc, exec, s[36:37]
	s_cbranch_vccnz .LBB0_2017
	s_ashr_i32 s36, s29, 5
	s_ashr_i32 s37, s36, 31
	s_lshl_b64 s[40:41], s[36:37], 12
	v_pk_mul_f32 v[168:169], v[156:157], v[128:129] op_sel_hi:[0,1]
	v_pk_mul_f32 v[166:167], v[156:157], v[126:127] op_sel_hi:[0,1]
	v_pk_mul_f32 v[170:171], v[156:157], v[124:125] op_sel_hi:[0,1]
	v_pk_mul_f32 v[172:173], v[156:157], v[122:123] op_sel_hi:[0,1]
	s_add_u32 s40, s44, s40
	v_lshlrev_b32_e32 v145, 6, v160
	v_cvt_pk_bf16_f32 v166, v166, v167
	v_cvt_pk_bf16_f32 v167, v168, v169
	v_cvt_pk_bf16_f32 v168, v172, v173
	v_cvt_pk_bf16_f32 v169, v170, v171
	s_addc_u32 s41, s45, s41
	v_lshl_or_b32 v145, v0, 4, v145
	s_or_b32 s36, s36, 1
	global_store_dwordx4 v145, v[166:169], s[40:41] sc1 nt
	v_pk_mul_f32 v[170:171], v[154:155], v[108:109] op_sel_hi:[0,1]
	v_pk_mul_f32 v[172:173], v[154:155], v[106:107] op_sel_hi:[0,1]
	v_pk_mul_f32 v[168:169], v[154:155], v[116:117] op_sel_hi:[0,1]
	v_pk_mul_f32 v[166:167], v[154:155], v[114:115] op_sel_hi:[0,1]
	s_ashr_i32 s37, s36, 31
	v_cvt_pk_bf16_f32 v166, v166, v167
	v_cvt_pk_bf16_f32 v167, v168, v169
	v_cvt_pk_bf16_f32 v168, v172, v173
	v_cvt_pk_bf16_f32 v169, v170, v171
	s_lshl_b64 s[36:37], s[36:37], 12
	global_store_dwordx4 v145, v[166:169], s[40:41] offset:256 sc1 nt
	v_pk_mul_f32 v[170:171], v[152:153], v[92:93] op_sel_hi:[0,1]
	v_pk_mul_f32 v[172:173], v[152:153], v[90:91] op_sel_hi:[0,1]
	v_pk_mul_f32 v[168:169], v[152:153], v[100:101] op_sel_hi:[0,1]
	v_pk_mul_f32 v[166:167], v[152:153], v[98:99] op_sel_hi:[0,1]
	s_add_u32 s36, s44, s36
	v_cvt_pk_bf16_f32 v166, v166, v167
	v_cvt_pk_bf16_f32 v167, v168, v169
	v_cvt_pk_bf16_f32 v168, v172, v173
	v_cvt_pk_bf16_f32 v169, v170, v171
	s_addc_u32 s37, s45, s37
	global_store_dwordx4 v145, v[166:169], s[36:37] sc1 nt
	v_or_b32_e32 v0, 48, v158
	v_pk_mul_f32 v[170:171], v[150:151], v[76:77] op_sel_hi:[0,1]
	v_pk_mul_f32 v[168:169], v[150:151], v[84:85] op_sel_hi:[0,1]
	v_pk_mul_f32 v[166:167], v[150:151], v[82:83] op_sel_hi:[0,1]
	v_cvt_pk_bf16_f32 v166, v166, v167
	v_cvt_pk_bf16_f32 v167, v168, v169
	v_cvt_pk_bf16_f32 v169, v170, v171
	v_ashrrev_i32_e32 v170, 5, v0
	v_lshlrev_b32_e32 v143, 5, v160
	v_ashrrev_i32_e32 v171, 31, v170
	v_lshlrev_b32_e32 v0, 3, v0
	s_movk_i32 s40, 0xf8
	s_add_i32 s36, s29, 0x80
	v_lshlrev_b64 v[170:171], 12, v[170:171]
	v_and_or_b32 v0, v0, s40, v143
	s_ashr_i32 s36, s36, 5
	v_pk_mul_f32 v[172:173], v[150:151], v[74:75] op_sel_hi:[0,1]
	v_lshl_add_u64 v[170:171], s[44:45], 0, v[170:171]
	v_lshlrev_b32_e32 v0, 1, v0
	s_ashr_i32 s37, s36, 31
	v_cvt_pk_bf16_f32 v168, v172, v173
	v_lshl_add_u64 v[170:171], v[170:171], 0, v[0:1]
	s_lshl_b64 s[36:37], s[36:37], 12
	global_store_dwordx4 v[170:171], v[166:169], off sc1 nt
	v_pk_mul_f32 v[170:171], v[148:149], v[60:61] op_sel_hi:[0,1]
	v_pk_mul_f32 v[172:173], v[148:149], v[58:59] op_sel_hi:[0,1]
	v_pk_mul_f32 v[168:169], v[148:149], v[64:65] op_sel_hi:[0,1]
	v_pk_mul_f32 v[166:167], v[148:149], v[62:63] op_sel_hi:[0,1]
	s_add_u32 s36, s44, s36
	v_cvt_pk_bf16_f32 v166, v166, v167
	v_cvt_pk_bf16_f32 v167, v168, v169
	v_cvt_pk_bf16_f32 v168, v172, v173
	v_cvt_pk_bf16_f32 v169, v170, v171
	s_addc_u32 s37, s45, s37
	global_store_dwordx4 v145, v[166:169], s[36:37] sc1 nt
	v_add_u32_e32 v0, 0x90, v158
	v_pk_mul_f32 v[170:171], v[146:147], v[48:49] op_sel_hi:[0,1]
	v_pk_mul_f32 v[168:169], v[146:147], v[56:57] op_sel_hi:[0,1]
	v_pk_mul_f32 v[166:167], v[146:147], v[54:55] op_sel_hi:[0,1]
	v_cvt_pk_bf16_f32 v166, v166, v167
	v_cvt_pk_bf16_f32 v167, v168, v169
	v_cvt_pk_bf16_f32 v169, v170, v171
	v_ashrrev_i32_e32 v170, 5, v0
	v_ashrrev_i32_e32 v171, 31, v170
	v_lshlrev_b32_e32 v0, 3, v0
	s_addk_i32 s29, 0xa0
	v_lshlrev_b64 v[170:171], 12, v[170:171]
	v_and_or_b32 v0, v0, s40, v143
	s_ashr_i32 s36, s29, 5
	v_pk_mul_f32 v[172:173], v[146:147], v[46:47] op_sel_hi:[0,1]
	v_lshl_add_u64 v[170:171], s[44:45], 0, v[170:171]
	v_lshlrev_b32_e32 v0, 1, v0
	s_ashr_i32 s37, s36, 31
	v_cvt_pk_bf16_f32 v168, v172, v173
	v_lshl_add_u64 v[170:171], v[170:171], 0, v[0:1]
	s_lshl_b64 s[36:37], s[36:37], 12
	global_store_dwordx4 v[170:171], v[166:169], off sc1 nt
	v_pk_mul_f32 v[170:171], v[144:145], v[32:33] op_sel_hi:[0,1]
	v_pk_mul_f32 v[172:173], v[144:145], v[30:31] op_sel_hi:[0,1]
	v_pk_mul_f32 v[168:169], v[144:145], v[40:41] op_sel_hi:[0,1]
	v_pk_mul_f32 v[166:167], v[144:145], v[38:39] op_sel_hi:[0,1]
	s_add_u32 s36, s44, s36
	v_cvt_pk_bf16_f32 v166, v166, v167
	v_cvt_pk_bf16_f32 v167, v168, v169
	v_cvt_pk_bf16_f32 v168, v172, v173
	v_cvt_pk_bf16_f32 v169, v170, v171
	s_addc_u32 s37, s45, s37
	global_store_dwordx4 v145, v[166:169], s[36:37] sc1 nt
	v_add_u32_e32 v0, 0xb0, v158
	v_pk_mul_f32 v[170:171], v[142:143], v[16:17] op_sel_hi:[0,1]
	v_pk_mul_f32 v[168:169], v[142:143], v[24:25] op_sel_hi:[0,1]
	v_pk_mul_f32 v[166:167], v[142:143], v[22:23] op_sel_hi:[0,1]
	v_cvt_pk_bf16_f32 v166, v166, v167
	v_cvt_pk_bf16_f32 v167, v168, v169
	v_cvt_pk_bf16_f32 v169, v170, v171
	v_ashrrev_i32_e32 v170, 5, v0
	v_ashrrev_i32_e32 v171, 31, v170
	v_lshlrev_b32_e32 v0, 3, v0
	v_lshlrev_b64 v[170:171], 12, v[170:171]
	v_and_or_b32 v0, v0, s40, v143
	v_pk_mul_f32 v[172:173], v[142:143], v[14:15] op_sel_hi:[0,1]
	v_lshl_add_u64 v[170:171], s[44:45], 0, v[170:171]
	v_lshlrev_b32_e32 v0, 1, v0
	v_cvt_pk_bf16_f32 v168, v172, v173
	v_lshl_add_u64 v[170:171], v[170:171], 0, v[0:1]
	global_store_dwordx4 v[170:171], v[166:169], off sc1 nt

.LBB0_2018:
	s_andn2_b64 vcc, exec, s[36:37]
	s_cbranch_vccnz .LBB0_2020
	s_lshl_b32 s29, s50, 8
	s_add_u32 s36, s74, s29
	s_addc_u32 s37, s75, 0
	v_lshlrev_b32_e32 v0, 1, v160
	v_lshl_add_u64 v[166:167], s[36:37], 0, v[0:1]
	s_mov_b64 s[36:37], 0xd7ff000
	v_lshl_add_u64 v[170:171], v[166:167], 0, s[36:37]
	v_mul_f32_e32 v0, v156, v156
	v_pk_mul_f32 v[166:167], v[128:129], v[120:121]
	v_pk_mul_f32 v[168:169], v[126:127], v[118:119]
	v_pk_mul_f32 v[172:173], v[0:1], v[166:167] op_sel_hi:[0,1]
	v_pk_mul_f32 v[166:167], v[0:1], v[168:169] op_sel_hi:[0,1]
	v_pk_mul_f32 v[168:169], v[124:125], v[112:113]
	v_pk_mul_f32 v[174:175], v[122:123], v[110:111]
	v_ashrrev_i32_e32 v159, 31, v158
	v_pk_mul_f32 v[176:177], v[0:1], v[168:169] op_sel_hi:[0,1]
	v_pk_mul_f32 v[168:169], v[0:1], v[174:175] op_sel_hi:[0,1]
	v_cvt_pk_bf16_f32 v166, v166, v167
	v_cvt_pk_bf16_f32 v167, v172, v173
	v_lshlrev_b64 v[172:173], 10, v[158:159]
	v_cvt_pk_bf16_f32 v168, v168, v169
	v_cvt_pk_bf16_f32 v169, v176, v177
	v_lshl_add_u64 v[172:173], v[170:171], 0, v[172:173]
	global_store_dwordx4 v[172:173], v[166:169], off sc1 nt
	v_mul_f32_e32 v0, v154, v154
	v_pk_mul_f32 v[176:177], v[106:107], v[94:95]
	v_pk_mul_f32 v[166:167], v[116:117], v[104:105]
	v_pk_mul_f32 v[168:169], v[114:115], v[102:103]
	v_pk_mul_f32 v[174:175], v[0:1], v[166:167] op_sel_hi:[0,1]
	v_pk_mul_f32 v[166:167], v[0:1], v[168:169] op_sel_hi:[0,1]
	v_cvt_pk_bf16_f32 v166, v166, v167
	v_cvt_pk_bf16_f32 v167, v174, v175
	v_or_b32_e32 v174, 16, v158
	v_pk_mul_f32 v[168:169], v[108:109], v[96:97]
	v_ashrrev_i32_e32 v175, 31, v174
	v_pk_mul_f32 v[178:179], v[0:1], v[168:169] op_sel_hi:[0,1]
	v_pk_mul_f32 v[168:169], v[0:1], v[176:177] op_sel_hi:[0,1]
	v_lshlrev_b64 v[174:175], 10, v[174:175]
	v_cvt_pk_bf16_f32 v168, v168, v169
	v_cvt_pk_bf16_f32 v169, v178, v179
	v_lshl_add_u64 v[174:175], v[170:171], 0, v[174:175]
	global_store_dwordx4 v[174:175], v[166:169], off sc1 nt
	v_mul_f32_e32 v0, v152, v152
	v_pk_mul_f32 v[176:177], v[90:91], v[78:79]
	v_pk_mul_f32 v[166:167], v[100:101], v[88:89]
	v_pk_mul_f32 v[168:169], v[98:99], v[86:87]
	v_pk_mul_f32 v[174:175], v[0:1], v[166:167] op_sel_hi:[0,1]
	v_pk_mul_f32 v[166:167], v[0:1], v[168:169] op_sel_hi:[0,1]
	v_cvt_pk_bf16_f32 v166, v166, v167
	v_cvt_pk_bf16_f32 v167, v174, v175
	v_or_b32_e32 v174, 32, v158
	v_pk_mul_f32 v[168:169], v[92:93], v[80:81]
	v_ashrrev_i32_e32 v175, 31, v174
	v_pk_mul_f32 v[178:179], v[0:1], v[168:169] op_sel_hi:[0,1]
	v_pk_mul_f32 v[168:169], v[0:1], v[176:177] op_sel_hi:[0,1]
	v_lshlrev_b64 v[174:175], 10, v[174:175]
	v_cvt_pk_bf16_f32 v168, v168, v169
	v_cvt_pk_bf16_f32 v169, v178, v179
	v_lshl_add_u64 v[174:175], v[170:171], 0, v[174:175]
	global_store_dwordx4 v[174:175], v[166:169], off sc1 nt
	v_mul_f32_e32 v0, v150, v150
	v_pk_mul_f32 v[176:177], v[74:75], v[66:67]
	v_pk_mul_f32 v[166:167], v[84:85], v[72:73]
	v_pk_mul_f32 v[168:169], v[82:83], v[70:71]
	v_pk_mul_f32 v[174:175], v[0:1], v[166:167] op_sel_hi:[0,1]
	v_pk_mul_f32 v[166:167], v[0:1], v[168:169] op_sel_hi:[0,1]
	v_cvt_pk_bf16_f32 v166, v166, v167
	v_cvt_pk_bf16_f32 v167, v174, v175
	v_or_b32_e32 v174, 48, v158
	v_pk_mul_f32 v[168:169], v[76:77], v[68:69]
	v_ashrrev_i32_e32 v175, 31, v174
	v_pk_mul_f32 v[178:179], v[0:1], v[168:169] op_sel_hi:[0,1]
	v_pk_mul_f32 v[168:169], v[0:1], v[176:177] op_sel_hi:[0,1]
	v_lshlrev_b64 v[174:175], 10, v[174:175]
	v_cvt_pk_bf16_f32 v168, v168, v169
	v_cvt_pk_bf16_f32 v169, v178, v179
	v_lshl_add_u64 v[170:171], v[170:171], 0, v[174:175]
	global_store_dwordx4 v[170:171], v[166:169], off sc1 nt
	v_mul_f32_e32 v0, v148, v148
	v_pk_mul_f32 v[174:175], v[58:59], v[42:43]
	v_pk_mul_f32 v[166:167], v[64:65], v[52:53]
	v_pk_mul_f32 v[168:169], v[62:63], v[50:51]
	v_pk_mul_f32 v[170:171], v[0:1], v[166:167] op_sel_hi:[0,1]
	v_pk_mul_f32 v[166:167], v[0:1], v[168:169] op_sel_hi:[0,1]
	v_pk_mul_f32 v[168:169], v[60:61], v[44:45]
	s_mov_b32 s29, 0x20000
	v_pk_mul_f32 v[176:177], v[0:1], v[168:169] op_sel_hi:[0,1]
	v_pk_mul_f32 v[168:169], v[0:1], v[174:175] op_sel_hi:[0,1]
	v_cvt_pk_bf16_f32 v166, v166, v167
	v_cvt_pk_bf16_f32 v167, v170, v171
	v_add_co_u32_e32 v170, vcc, s29, v172
	v_cvt_pk_bf16_f32 v168, v168, v169
	v_cvt_pk_bf16_f32 v169, v176, v177
	v_addc_co_u32_e32 v171, vcc, 0, v173, vcc
	global_store_dwordx4 v[170:171], v[166:169], off sc1 nt
	v_mul_f32_e32 v0, v146, v146
	v_pk_mul_f32 v[174:175], v[46:47], v[26:27]
	v_pk_mul_f32 v[166:167], v[56:57], v[36:37]
	v_pk_mul_f32 v[168:169], v[54:55], v[34:35]
	v_pk_mul_f32 v[170:171], v[0:1], v[166:167] op_sel_hi:[0,1]
	v_pk_mul_f32 v[166:167], v[0:1], v[168:169] op_sel_hi:[0,1]
	v_pk_mul_f32 v[168:169], v[48:49], v[28:29]
	s_mov_b32 s29, 0x24000
	v_pk_mul_f32 v[176:177], v[0:1], v[168:169] op_sel_hi:[0,1]
	v_pk_mul_f32 v[168:169], v[0:1], v[174:175] op_sel_hi:[0,1]
	v_cvt_pk_bf16_f32 v166, v166, v167
	v_cvt_pk_bf16_f32 v167, v170, v171
	v_add_co_u32_e32 v170, vcc, s29, v172
	v_cvt_pk_bf16_f32 v168, v168, v169
	v_cvt_pk_bf16_f32 v169, v176, v177
	v_addc_co_u32_e32 v171, vcc, 0, v173, vcc
	global_store_dwordx4 v[170:171], v[166:169], off sc1 nt
	v_mul_f32_e32 v0, v144, v144
	v_pk_mul_f32 v[174:175], v[30:31], v[10:11]
	v_pk_mul_f32 v[166:167], v[40:41], v[20:21]
	v_pk_mul_f32 v[168:169], v[38:39], v[18:19]
	v_pk_mul_f32 v[170:171], v[0:1], v[166:167] op_sel_hi:[0,1]
	v_pk_mul_f32 v[166:167], v[0:1], v[168:169] op_sel_hi:[0,1]
	v_pk_mul_f32 v[168:169], v[32:33], v[12:13]
	s_mov_b32 s29, 0x28000
	v_pk_mul_f32 v[176:177], v[0:1], v[168:169] op_sel_hi:[0,1]
	v_pk_mul_f32 v[168:169], v[0:1], v[174:175] op_sel_hi:[0,1]
	v_cvt_pk_bf16_f32 v166, v166, v167
	v_cvt_pk_bf16_f32 v167, v170, v171
	v_add_co_u32_e32 v170, vcc, s29, v172
	v_cvt_pk_bf16_f32 v168, v168, v169
	v_cvt_pk_bf16_f32 v169, v176, v177
	v_addc_co_u32_e32 v171, vcc, 0, v173, vcc
	global_store_dwordx4 v[170:171], v[166:169], off sc1 nt
	v_mul_f32_e32 v0, v142, v142
	v_pk_mul_f32 v[174:175], v[14:15], v[2:3]
	v_pk_mul_f32 v[166:167], v[24:25], v[8:9]
	v_pk_mul_f32 v[168:169], v[22:23], v[6:7]
	v_pk_mul_f32 v[170:171], v[0:1], v[166:167] op_sel_hi:[0,1]
	v_pk_mul_f32 v[166:167], v[0:1], v[168:169] op_sel_hi:[0,1]
	v_pk_mul_f32 v[168:169], v[16:17], v[4:5]
	v_cvt_pk_bf16_f32 v166, v166, v167
	v_pk_mul_f32 v[176:177], v[0:1], v[168:169] op_sel_hi:[0,1]
	v_pk_mul_f32 v[168:169], v[0:1], v[174:175] op_sel_hi:[0,1]
	v_cvt_pk_bf16_f32 v167, v170, v171
	v_add_co_u32_e32 v170, vcc, 0x2c000, v172
	v_cvt_pk_bf16_f32 v168, v168, v169
	v_cvt_pk_bf16_f32 v169, v176, v177
	v_addc_co_u32_e32 v171, vcc, 0, v173, vcc
	global_store_dwordx4 v[170:171], v[166:169], off sc1 nt

.LBB0_2042:
	s_cmp_eq_u32 s29, 3
	s_cselect_b64 s[40:41], -1, 0
	s_or_b64 vcc, s[36:37], s[40:41]
	s_add_u32 s29, s74, s60
	s_addc_u32 s37, s75, s61
	s_lshl_b32 s36, s50, 9
	s_and_b32 s36, s36, 0x200
	v_mov_b32_e32 v0, 0x3e38aa3b
	s_add_u32 s36, s29, s36
	v_cndmask_b32_e32 v143, 1.0, v0, vcc
	s_addc_u32 s37, s37, 0
	v_lshlrev_b32_e32 v0, 1, v160
	v_lshl_add_u64 v[166:167], s[36:37], 0, v[0:1]
	v_ashrrev_i32_e32 v159, 31, v158
	v_mul_f32_e32 v0, v143, v156
	v_lshlrev_b64 v[160:161], 10, v[158:159]
	v_pk_mul_f32 v[128:129], v[0:1], v[128:129] op_sel_hi:[0,1]
	v_pk_mul_f32 v[126:127], v[0:1], v[126:127] op_sel_hi:[0,1]
	v_pk_mul_f32 v[156:157], v[0:1], v[124:125] op_sel_hi:[0,1]
	v_pk_mul_f32 v[124:125], v[0:1], v[122:123] op_sel_hi:[0,1]
	v_lshl_add_u64 v[160:161], v[166:167], 0, v[160:161]
	v_cvt_pk_bf16_f32 v122, v126, v127
	v_cvt_pk_bf16_f32 v123, v128, v129
	v_cvt_pk_bf16_f32 v124, v124, v125
	v_cvt_pk_bf16_f32 v125, v156, v157
	global_store_dwordx4 v[160:161], v[122:125], off sc1 nt
	v_pk_mul_f32 v[120:121], v[0:1], v[120:121] op_sel_hi:[0,1]
	v_pk_mul_f32 v[118:119], v[0:1], v[118:119] op_sel_hi:[0,1]
	v_pk_mul_f32 v[122:123], v[0:1], v[112:113] op_sel_hi:[0,1]
	v_pk_mul_f32 v[112:113], v[0:1], v[110:111] op_sel_hi:[0,1]
	v_cvt_pk_bf16_f32 v110, v118, v119
	v_cvt_pk_bf16_f32 v111, v120, v121
	v_cvt_pk_bf16_f32 v112, v112, v113
	v_cvt_pk_bf16_f32 v113, v122, v123
	global_store_dwordx4 v[160:161], v[110:113], off offset:256 sc1 nt
	v_mul_f32_e32 v0, v143, v154
	v_pk_mul_f32 v[114:115], v[0:1], v[114:115] op_sel_hi:[0,1]
	v_or_b32_e32 v110, 16, v158
	v_ashrrev_i32_e32 v111, 31, v110
	v_lshlrev_b64 v[110:111], 10, v[110:111]
	v_pk_mul_f32 v[112:113], v[0:1], v[116:117] op_sel_hi:[0,1]
	v_pk_mul_f32 v[116:117], v[0:1], v[108:109] op_sel_hi:[0,1]
	v_pk_mul_f32 v[108:109], v[0:1], v[106:107] op_sel_hi:[0,1]
	v_lshl_add_u64 v[110:111], v[166:167], 0, v[110:111]
	v_cvt_pk_bf16_f32 v106, v114, v115
	v_cvt_pk_bf16_f32 v107, v112, v113
	v_cvt_pk_bf16_f32 v108, v108, v109
	v_cvt_pk_bf16_f32 v109, v116, v117
	global_store_dwordx4 v[110:111], v[106:109], off sc1 nt
	v_pk_mul_f32 v[104:105], v[0:1], v[104:105] op_sel_hi:[0,1]
	v_pk_mul_f32 v[102:103], v[0:1], v[102:103] op_sel_hi:[0,1]
	v_pk_mul_f32 v[106:107], v[0:1], v[96:97] op_sel_hi:[0,1]
	v_pk_mul_f32 v[96:97], v[0:1], v[94:95] op_sel_hi:[0,1]
	v_cvt_pk_bf16_f32 v94, v102, v103
	v_cvt_pk_bf16_f32 v95, v104, v105
	v_cvt_pk_bf16_f32 v96, v96, v97
	v_cvt_pk_bf16_f32 v97, v106, v107
	global_store_dwordx4 v[110:111], v[94:97], off offset:256 sc1 nt
	v_mul_f32_e32 v0, v143, v152
	v_pk_mul_f32 v[98:99], v[0:1], v[98:99] op_sel_hi:[0,1]
	v_or_b32_e32 v94, 32, v158
	v_ashrrev_i32_e32 v95, 31, v94
	v_lshlrev_b64 v[94:95], 10, v[94:95]
	v_pk_mul_f32 v[96:97], v[0:1], v[100:101] op_sel_hi:[0,1]
	v_pk_mul_f32 v[100:101], v[0:1], v[92:93] op_sel_hi:[0,1]
	v_pk_mul_f32 v[92:93], v[0:1], v[90:91] op_sel_hi:[0,1]
	v_lshl_add_u64 v[94:95], v[166:167], 0, v[94:95]
	v_cvt_pk_bf16_f32 v90, v98, v99
	v_cvt_pk_bf16_f32 v91, v96, v97
	v_cvt_pk_bf16_f32 v92, v92, v93
	v_cvt_pk_bf16_f32 v93, v100, v101
	global_store_dwordx4 v[94:95], v[90:93], off sc1 nt
	v_pk_mul_f32 v[88:89], v[0:1], v[88:89] op_sel_hi:[0,1]
	v_pk_mul_f32 v[86:87], v[0:1], v[86:87] op_sel_hi:[0,1]
	v_pk_mul_f32 v[90:91], v[0:1], v[80:81] op_sel_hi:[0,1]
	v_pk_mul_f32 v[80:81], v[0:1], v[78:79] op_sel_hi:[0,1]
	v_cvt_pk_bf16_f32 v78, v86, v87
	v_cvt_pk_bf16_f32 v79, v88, v89
	v_cvt_pk_bf16_f32 v80, v80, v81
	v_cvt_pk_bf16_f32 v81, v90, v91
	global_store_dwordx4 v[94:95], v[78:81], off offset:256 sc1 nt
	v_mul_f32_e32 v0, v143, v150
	v_pk_mul_f32 v[82:83], v[0:1], v[82:83] op_sel_hi:[0,1]
	v_or_b32_e32 v78, 48, v158
	v_ashrrev_i32_e32 v79, 31, v78
	v_lshlrev_b64 v[78:79], 10, v[78:79]
	v_pk_mul_f32 v[80:81], v[0:1], v[84:85] op_sel_hi:[0,1]
	v_pk_mul_f32 v[84:85], v[0:1], v[76:77] op_sel_hi:[0,1]
	v_pk_mul_f32 v[76:77], v[0:1], v[74:75] op_sel_hi:[0,1]
	v_lshl_add_u64 v[78:79], v[166:167], 0, v[78:79]
	v_cvt_pk_bf16_f32 v74, v82, v83
	v_cvt_pk_bf16_f32 v75, v80, v81
	v_cvt_pk_bf16_f32 v76, v76, v77
	v_cvt_pk_bf16_f32 v77, v84, v85
	global_store_dwordx4 v[78:79], v[74:77], off sc1 nt
	v_pk_mul_f32 v[72:73], v[0:1], v[72:73] op_sel_hi:[0,1]
	v_pk_mul_f32 v[70:71], v[0:1], v[70:71] op_sel_hi:[0,1]
	v_pk_mul_f32 v[74:75], v[0:1], v[68:69] op_sel_hi:[0,1]
	v_pk_mul_f32 v[68:69], v[0:1], v[66:67] op_sel_hi:[0,1]
	v_mul_f32_e32 v0, v143, v148
	v_cvt_pk_bf16_f32 v66, v70, v71
	v_cvt_pk_bf16_f32 v67, v72, v73
	v_cvt_pk_bf16_f32 v68, v68, v69
	v_cvt_pk_bf16_f32 v69, v74, v75
	v_pk_mul_f32 v[62:63], v[0:1], v[62:63] op_sel_hi:[0,1]
	s_mov_b32 s29, 0x20000
	global_store_dwordx4 v[78:79], v[66:69], off offset:256 sc1 nt
	v_pk_mul_f32 v[64:65], v[0:1], v[64:65] op_sel_hi:[0,1]
	v_pk_mul_f32 v[52:53], v[0:1], v[52:53] op_sel_hi:[0,1]
	v_pk_mul_f32 v[68:69], v[0:1], v[60:61] op_sel_hi:[0,1]
	v_pk_mul_f32 v[60:61], v[0:1], v[58:59] op_sel_hi:[0,1]
	v_cvt_pk_bf16_f32 v58, v62, v63
	v_add_co_u32_e32 v62, vcc, s29, v160
	v_cvt_pk_bf16_f32 v59, v64, v65
	v_cvt_pk_bf16_f32 v60, v60, v61
	v_cvt_pk_bf16_f32 v61, v68, v69
	v_addc_co_u32_e32 v63, vcc, 0, v161, vcc
	global_store_dwordx4 v[62:63], v[58:61], off sc1 nt
	v_pk_mul_f32 v[50:51], v[0:1], v[50:51] op_sel_hi:[0,1]
	v_lshl_add_u64 v[66:67], v[160:161], 0, s[24:25]
	v_pk_mul_f32 v[58:59], v[0:1], v[44:45] op_sel_hi:[0,1]
	v_pk_mul_f32 v[44:45], v[0:1], v[42:43] op_sel_hi:[0,1]
	v_cvt_pk_bf16_f32 v42, v50, v51
	v_cvt_pk_bf16_f32 v43, v52, v53
	v_cvt_pk_bf16_f32 v44, v44, v45
	v_cvt_pk_bf16_f32 v45, v58, v59
	v_mul_f32_e32 v0, v143, v146
	global_store_dwordx4 v[66:67], v[42:45], off offset:256 sc1 nt
	v_pk_mul_f32 v[46:47], v[0:1], v[46:47] op_sel_hi:[0,1]
	s_mov_b32 s29, 0x24000
	v_pk_mul_f32 v[44:45], v[0:1], v[56:57] op_sel_hi:[0,1]
	v_pk_mul_f32 v[42:43], v[0:1], v[54:55] op_sel_hi:[0,1]
	v_pk_mul_f32 v[48:49], v[0:1], v[48:49] op_sel_hi:[0,1]
	v_cvt_pk_bf16_f32 v42, v42, v43
	v_cvt_pk_bf16_f32 v43, v44, v45
	v_cvt_pk_bf16_f32 v44, v46, v47
	v_add_co_u32_e32 v46, vcc, s29, v160
	v_cvt_pk_bf16_f32 v45, v48, v49
	s_nop 0
	v_addc_co_u32_e32 v47, vcc, 0, v161, vcc
	s_mov_b64 s[36:37], 0x24000
	global_store_dwordx4 v[46:47], v[42:45], off sc1 nt
	v_pk_mul_f32 v[36:37], v[0:1], v[36:37] op_sel_hi:[0,1]
	v_pk_mul_f32 v[34:35], v[0:1], v[34:35] op_sel_hi:[0,1]
	v_pk_mul_f32 v[42:43], v[0:1], v[28:29] op_sel_hi:[0,1]
	v_pk_mul_f32 v[28:29], v[0:1], v[26:27] op_sel_hi:[0,1]
	v_lshl_add_u64 v[50:51], v[160:161], 0, s[36:37]
	v_cvt_pk_bf16_f32 v26, v34, v35
	v_cvt_pk_bf16_f32 v27, v36, v37
	v_cvt_pk_bf16_f32 v28, v28, v29
	v_cvt_pk_bf16_f32 v29, v42, v43
	v_mul_f32_e32 v0, v143, v144
	global_store_dwordx4 v[50:51], v[26:29], off offset:256 sc1 nt
	v_pk_mul_f32 v[30:31], v[0:1], v[30:31] op_sel_hi:[0,1]
	s_mov_b32 s29, 0x28000
	v_pk_mul_f32 v[28:29], v[0:1], v[40:41] op_sel_hi:[0,1]
	v_pk_mul_f32 v[26:27], v[0:1], v[38:39] op_sel_hi:[0,1]
	v_pk_mul_f32 v[32:33], v[0:1], v[32:33] op_sel_hi:[0,1]
	v_cvt_pk_bf16_f32 v26, v26, v27
	v_cvt_pk_bf16_f32 v27, v28, v29
	v_cvt_pk_bf16_f32 v28, v30, v31
	v_add_co_u32_e32 v30, vcc, s29, v160
	v_cvt_pk_bf16_f32 v29, v32, v33
	s_nop 0
	v_addc_co_u32_e32 v31, vcc, 0, v161, vcc
	s_mov_b64 s[36:37], 0x28000
	global_store_dwordx4 v[30:31], v[26:29], off sc1 nt
	v_pk_mul_f32 v[20:21], v[0:1], v[20:21] op_sel_hi:[0,1]
	v_pk_mul_f32 v[18:19], v[0:1], v[18:19] op_sel_hi:[0,1]
	v_pk_mul_f32 v[26:27], v[0:1], v[12:13] op_sel_hi:[0,1]
	v_pk_mul_f32 v[12:13], v[0:1], v[10:11] op_sel_hi:[0,1]
	v_lshl_add_u64 v[34:35], v[160:161], 0, s[36:37]
	v_cvt_pk_bf16_f32 v10, v18, v19
	v_cvt_pk_bf16_f32 v11, v20, v21
	v_cvt_pk_bf16_f32 v12, v12, v13
	v_cvt_pk_bf16_f32 v13, v26, v27
	v_mul_f32_e32 v0, v143, v142
	global_store_dwordx4 v[34:35], v[10:13], off offset:256 sc1 nt
	v_pk_mul_f32 v[14:15], v[0:1], v[14:15] op_sel_hi:[0,1]
	s_mov_b32 s29, 0x2c000
	v_pk_mul_f32 v[12:13], v[0:1], v[24:25] op_sel_hi:[0,1]
	v_pk_mul_f32 v[10:11], v[0:1], v[22:23] op_sel_hi:[0,1]
	v_pk_mul_f32 v[16:17], v[0:1], v[16:17] op_sel_hi:[0,1]
	v_cvt_pk_bf16_f32 v10, v10, v11
	v_cvt_pk_bf16_f32 v11, v12, v13
	v_cvt_pk_bf16_f32 v12, v14, v15
	v_add_co_u32_e32 v14, vcc, s29, v160
	v_cvt_pk_bf16_f32 v13, v16, v17
	s_nop 0
	v_addc_co_u32_e32 v15, vcc, 0, v161, vcc
	s_mov_b64 s[36:37], 0x2c000
	global_store_dwordx4 v[14:15], v[10:13], off sc1 nt
	v_pk_mul_f32 v[8:9], v[0:1], v[8:9] op_sel_hi:[0,1]
	v_pk_mul_f32 v[6:7], v[0:1], v[6:7] op_sel_hi:[0,1]
	v_pk_mul_f32 v[10:11], v[0:1], v[4:5] op_sel_hi:[0,1]
	v_pk_mul_f32 v[4:5], v[0:1], v[2:3] op_sel_hi:[0,1]
	v_lshl_add_u64 v[18:19], v[160:161], 0, s[36:37]
	v_cvt_pk_bf16_f32 v2, v6, v7
	v_cvt_pk_bf16_f32 v3, v8, v9
	v_cvt_pk_bf16_f32 v4, v4, v5
	v_cvt_pk_bf16_f32 v5, v10, v11
	global_store_dwordx4 v[18:19], v[2:5], off offset:256 sc1 nt
